# worker GCN1 loop instruction diet (SGPR-base DMA addressing, unmasked index loads + select), fma_mix accumulate, L1 last-step code out of line
# speedup vs baseline: 1.0415x; 1.0188x over previous
.LBB1_310:
	v_lshl_or_b32 v56, s16, 3, v19
	v_add_u32_e32 v2, s22, v56
	v_ashrrev_i32_e32 v3, 31, v2
	v_lshlrev_b64 v[4:5], 2, v[2:3]
	v_lshl_add_u64 v[6:7], s[46:47], 0, v[4:5]
	global_load_dwordx2 v[22:23], v[6:7], off
	v_lshlrev_b64 v[2:3], 7, v[2:3]
	v_lshl_add_u64 v[4:5], s[50:51], 0, v[4:5]
	v_lshl_add_u64 v[2:3], v[16:17], 0, v[2:3]
	global_load_dword v20, v[4:5], off
	global_load_dwordx4 v[12:15], v[2:3], off
	s_waitcnt vmcnt(2)
	v_sub_u32_e32 v57, v23, v22
	ds_bpermute_b32 v1, v11, v57
	v_cmp_lt_i32_e32 vcc, 0, v57
	v_ashrrev_i32_e32 v23, 31, v22
	s_waitcnt lgkmcnt(0)
	v_max_i32_e32 v1, v57, v1
	ds_bpermute_b32 v2, v21, v1
	s_waitcnt lgkmcnt(0)
	v_max_i32_e32 v24, v1, v2
	ds_bpermute_b32 v25, v54, v24
	v_lshlrev_b32_e32 v26, 2, v22
	v_mov_b32_e32 v30, 0x4e20
	global_load_dword v2, v26, s[48:49]
	global_load_dword v1, v26, s[48:49] offset:4
	global_load_dword v4, v26, s[48:49] offset:8
	global_load_dword v3, v26, s[48:49] offset:12
	global_load_dword v6, v26, s[48:49] offset:16
	global_load_dword v5, v26, s[48:49] offset:20
	global_load_dword v8, v26, s[48:49] offset:24
	global_load_dword v7, v26, s[48:49] offset:28
	global_load_dword v10, v26, s[48:49] offset:32
	global_load_dword v9, v26, s[48:49] offset:36
	s_waitcnt lgkmcnt(0)
	v_max_i32_e32 v23, v24, v25
	s_waitcnt vmcnt(0)
	v_cmp_lt_i32_e64 s[70:71], 0, v57
	v_cmp_lt_i32_e64 s[72:73], 1, v57
	v_cmp_lt_i32_e64 s[74:75], 2, v57
	v_cmp_lt_i32_e64 s[76:77], 3, v57
	v_cmp_lt_i32_e64 s[78:79], 4, v57
	v_cmp_lt_i32_e64 s[80:81], 5, v57
	v_cmp_lt_i32_e64 s[82:83], 6, v57
	v_cmp_lt_i32_e64 s[84:85], 7, v57
	v_cmp_lt_i32_e64 s[86:87], 8, v57
	v_cmp_lt_i32_e64 s[88:89], 9, v57
	v_cndmask_b32_e64 v2, v30, v2, s[70:71]
	v_cndmask_b32_e64 v1, v30, v1, s[72:73]
	v_cndmask_b32_e64 v4, v30, v4, s[74:75]
	v_cndmask_b32_e64 v3, v30, v3, s[76:77]
	v_cndmask_b32_e64 v6, v30, v6, s[78:79]
	v_cndmask_b32_e64 v5, v30, v5, s[80:81]
	v_cndmask_b32_e64 v8, v30, v8, s[82:83]
	v_cndmask_b32_e64 v7, v30, v7, s[84:85]
	v_cndmask_b32_e64 v10, v30, v10, s[86:87]
	v_cndmask_b32_e64 v9, v30, v9, s[88:89]
	v_cvt_f32_f16_sdwa v29, v12 dst_sel:DWORD dst_unused:UNUSED_PAD src0_sel:WORD_1
	v_cvt_f32_f16_e32 v28, v12
	v_cvt_f32_f16_sdwa v27, v13 dst_sel:DWORD dst_unused:UNUSED_PAD src0_sel:WORD_1
	v_cvt_f32_f16_e32 v26, v13
	v_cvt_f32_f16_sdwa v25, v14 dst_sel:DWORD dst_unused:UNUSED_PAD src0_sel:WORD_1
	v_cvt_f32_f16_e32 v24, v14
	v_cvt_f32_f16_sdwa v13, v15 dst_sel:DWORD dst_unused:UNUSED_PAD src0_sel:WORD_1
	v_cvt_f32_f16_e32 v12, v15
	v_readfirstlane_b32 s17, v23
	s_cmp_gt_i32 s17, 0
	s_cbranch_scc0 .LBB1_309
	v_and_b32_e32 v31, 7, v106
	v_lshlrev_b32_e32 v31, 4, v31
	s_mov_b32 s18, 19
	s_branch .LBB1_333
.LBB1_332:
	s_nop 0
	s_waitcnt vmcnt(0)
	s_waitcnt vmcnt(0)
	ds_read_b128 v[58:61], v55
	ds_read_b128 v[62:65], v55 offset:1024
	ds_read_b128 v[66:69], v55 offset:2048
	ds_read_b128 v[70:73], v55 offset:3072
	ds_read_b128 v[74:77], v55 offset:4096
	ds_read_b128 v[78:81], v55 offset:5120
	ds_read_b128 v[82:85], v55 offset:6144
	ds_read_b128 v[86:89], v55 offset:7168
	ds_read_b128 v[90:93], v55 offset:8192
	ds_read_b128 v[94:97], v55 offset:9216
	v_cmp_lt_i32_e64 s[70:71], 0, v15
	v_cmp_lt_i32_e64 s[72:73], 1, v15
	v_cmp_lt_i32_e64 s[74:75], 2, v15
	v_cmp_lt_i32_e64 s[76:77], 3, v15
	v_cmp_lt_i32_e64 s[78:79], 4, v15
	v_cmp_lt_i32_e64 s[80:81], 5, v15
	v_cmp_lt_i32_e64 s[82:83], 6, v15
	v_cmp_lt_i32_e64 s[84:85], 7, v15
	v_cmp_lt_i32_e64 s[86:87], 8, v15
	v_cmp_lt_i32_e64 s[88:89], 9, v15
	v_cndmask_b32_e64 v2, v30, v2, s[70:71]
	v_cndmask_b32_e64 v1, v30, v1, s[72:73]
	v_cndmask_b32_e64 v4, v30, v4, s[74:75]
	v_cndmask_b32_e64 v3, v30, v3, s[76:77]
	v_cndmask_b32_e64 v6, v30, v6, s[78:79]
	v_cndmask_b32_e64 v5, v30, v5, s[80:81]
	v_cndmask_b32_e64 v8, v30, v8, s[82:83]
	v_cndmask_b32_e64 v7, v30, v7, s[84:85]
	v_cndmask_b32_e64 v10, v30, v10, s[86:87]
	v_cndmask_b32_e64 v9, v30, v9, s[88:89]
	s_waitcnt lgkmcnt(0)
	v_fma_mix_f32 v28, v58, 1.0, v28 op_sel_hi:[1,0,0]
	v_fma_mix_f32 v29, v58, 1.0, v29 op_sel:[1,0,0] op_sel_hi:[1,0,0]
	v_fma_mix_f32 v26, v59, 1.0, v26 op_sel_hi:[1,0,0]
	v_fma_mix_f32 v27, v59, 1.0, v27 op_sel:[1,0,0] op_sel_hi:[1,0,0]
	v_fma_mix_f32 v24, v60, 1.0, v24 op_sel_hi:[1,0,0]
	v_fma_mix_f32 v25, v60, 1.0, v25 op_sel:[1,0,0] op_sel_hi:[1,0,0]
	v_fma_mix_f32 v12, v61, 1.0, v12 op_sel_hi:[1,0,0]
	v_fma_mix_f32 v13, v61, 1.0, v13 op_sel:[1,0,0] op_sel_hi:[1,0,0]
	v_fma_mix_f32 v28, v62, 1.0, v28 op_sel_hi:[1,0,0]
	v_fma_mix_f32 v29, v62, 1.0, v29 op_sel:[1,0,0] op_sel_hi:[1,0,0]
	v_fma_mix_f32 v26, v63, 1.0, v26 op_sel_hi:[1,0,0]
	v_fma_mix_f32 v27, v63, 1.0, v27 op_sel:[1,0,0] op_sel_hi:[1,0,0]
	v_fma_mix_f32 v24, v64, 1.0, v24 op_sel_hi:[1,0,0]
	v_fma_mix_f32 v25, v64, 1.0, v25 op_sel:[1,0,0] op_sel_hi:[1,0,0]
	v_fma_mix_f32 v12, v65, 1.0, v12 op_sel_hi:[1,0,0]
	v_fma_mix_f32 v13, v65, 1.0, v13 op_sel:[1,0,0] op_sel_hi:[1,0,0]
	v_fma_mix_f32 v28, v66, 1.0, v28 op_sel_hi:[1,0,0]
	v_fma_mix_f32 v29, v66, 1.0, v29 op_sel:[1,0,0] op_sel_hi:[1,0,0]
	v_fma_mix_f32 v26, v67, 1.0, v26 op_sel_hi:[1,0,0]
	v_fma_mix_f32 v27, v67, 1.0, v27 op_sel:[1,0,0] op_sel_hi:[1,0,0]
	v_fma_mix_f32 v24, v68, 1.0, v24 op_sel_hi:[1,0,0]
	v_fma_mix_f32 v25, v68, 1.0, v25 op_sel:[1,0,0] op_sel_hi:[1,0,0]
	v_fma_mix_f32 v12, v69, 1.0, v12 op_sel_hi:[1,0,0]
	v_fma_mix_f32 v13, v69, 1.0, v13 op_sel:[1,0,0] op_sel_hi:[1,0,0]
	v_fma_mix_f32 v28, v70, 1.0, v28 op_sel_hi:[1,0,0]
	v_fma_mix_f32 v29, v70, 1.0, v29 op_sel:[1,0,0] op_sel_hi:[1,0,0]
	v_fma_mix_f32 v26, v71, 1.0, v26 op_sel_hi:[1,0,0]
	v_fma_mix_f32 v27, v71, 1.0, v27 op_sel:[1,0,0] op_sel_hi:[1,0,0]
	v_fma_mix_f32 v24, v72, 1.0, v24 op_sel_hi:[1,0,0]
	v_fma_mix_f32 v25, v72, 1.0, v25 op_sel:[1,0,0] op_sel_hi:[1,0,0]
	v_fma_mix_f32 v12, v73, 1.0, v12 op_sel_hi:[1,0,0]
	v_fma_mix_f32 v13, v73, 1.0, v13 op_sel:[1,0,0] op_sel_hi:[1,0,0]
	v_fma_mix_f32 v28, v74, 1.0, v28 op_sel_hi:[1,0,0]
	v_fma_mix_f32 v29, v74, 1.0, v29 op_sel:[1,0,0] op_sel_hi:[1,0,0]
	v_fma_mix_f32 v26, v75, 1.0, v26 op_sel_hi:[1,0,0]
	v_fma_mix_f32 v27, v75, 1.0, v27 op_sel:[1,0,0] op_sel_hi:[1,0,0]
	v_fma_mix_f32 v24, v76, 1.0, v24 op_sel_hi:[1,0,0]
	v_fma_mix_f32 v25, v76, 1.0, v25 op_sel:[1,0,0] op_sel_hi:[1,0,0]
	v_fma_mix_f32 v12, v77, 1.0, v12 op_sel_hi:[1,0,0]
	v_fma_mix_f32 v13, v77, 1.0, v13 op_sel:[1,0,0] op_sel_hi:[1,0,0]
	v_fma_mix_f32 v28, v78, 1.0, v28 op_sel_hi:[1,0,0]
	v_fma_mix_f32 v29, v78, 1.0, v29 op_sel:[1,0,0] op_sel_hi:[1,0,0]
	v_fma_mix_f32 v26, v79, 1.0, v26 op_sel_hi:[1,0,0]
	v_fma_mix_f32 v27, v79, 1.0, v27 op_sel:[1,0,0] op_sel_hi:[1,0,0]
	v_fma_mix_f32 v24, v80, 1.0, v24 op_sel_hi:[1,0,0]
	v_fma_mix_f32 v25, v80, 1.0, v25 op_sel:[1,0,0] op_sel_hi:[1,0,0]
	v_fma_mix_f32 v12, v81, 1.0, v12 op_sel_hi:[1,0,0]
	v_fma_mix_f32 v13, v81, 1.0, v13 op_sel:[1,0,0] op_sel_hi:[1,0,0]
	v_fma_mix_f32 v28, v82, 1.0, v28 op_sel_hi:[1,0,0]
	v_fma_mix_f32 v29, v82, 1.0, v29 op_sel:[1,0,0] op_sel_hi:[1,0,0]
	v_fma_mix_f32 v26, v83, 1.0, v26 op_sel_hi:[1,0,0]
	v_fma_mix_f32 v27, v83, 1.0, v27 op_sel:[1,0,0] op_sel_hi:[1,0,0]
	v_fma_mix_f32 v24, v84, 1.0, v24 op_sel_hi:[1,0,0]
	v_fma_mix_f32 v25, v84, 1.0, v25 op_sel:[1,0,0] op_sel_hi:[1,0,0]
	v_fma_mix_f32 v12, v85, 1.0, v12 op_sel_hi:[1,0,0]
	v_fma_mix_f32 v13, v85, 1.0, v13 op_sel:[1,0,0] op_sel_hi:[1,0,0]
	v_fma_mix_f32 v28, v86, 1.0, v28 op_sel_hi:[1,0,0]
	v_fma_mix_f32 v29, v86, 1.0, v29 op_sel:[1,0,0] op_sel_hi:[1,0,0]
	v_fma_mix_f32 v26, v87, 1.0, v26 op_sel_hi:[1,0,0]
	v_fma_mix_f32 v27, v87, 1.0, v27 op_sel:[1,0,0] op_sel_hi:[1,0,0]
	v_fma_mix_f32 v24, v88, 1.0, v24 op_sel_hi:[1,0,0]
	v_fma_mix_f32 v25, v88, 1.0, v25 op_sel:[1,0,0] op_sel_hi:[1,0,0]
	v_fma_mix_f32 v12, v89, 1.0, v12 op_sel_hi:[1,0,0]
	v_fma_mix_f32 v13, v89, 1.0, v13 op_sel:[1,0,0] op_sel_hi:[1,0,0]
	v_fma_mix_f32 v28, v90, 1.0, v28 op_sel_hi:[1,0,0]
	v_fma_mix_f32 v29, v90, 1.0, v29 op_sel:[1,0,0] op_sel_hi:[1,0,0]
	v_fma_mix_f32 v26, v91, 1.0, v26 op_sel_hi:[1,0,0]
	v_fma_mix_f32 v27, v91, 1.0, v27 op_sel:[1,0,0] op_sel_hi:[1,0,0]
	v_fma_mix_f32 v24, v92, 1.0, v24 op_sel_hi:[1,0,0]
	v_fma_mix_f32 v25, v92, 1.0, v25 op_sel:[1,0,0] op_sel_hi:[1,0,0]
	v_fma_mix_f32 v12, v93, 1.0, v12 op_sel_hi:[1,0,0]
	v_fma_mix_f32 v13, v93, 1.0, v13 op_sel:[1,0,0] op_sel_hi:[1,0,0]
	v_fma_mix_f32 v28, v94, 1.0, v28 op_sel_hi:[1,0,0]
	v_fma_mix_f32 v29, v94, 1.0, v29 op_sel:[1,0,0] op_sel_hi:[1,0,0]
	v_fma_mix_f32 v26, v95, 1.0, v26 op_sel_hi:[1,0,0]
	v_fma_mix_f32 v27, v95, 1.0, v27 op_sel:[1,0,0] op_sel_hi:[1,0,0]
	v_fma_mix_f32 v24, v96, 1.0, v24 op_sel_hi:[1,0,0]
	v_fma_mix_f32 v25, v96, 1.0, v25 op_sel:[1,0,0] op_sel_hi:[1,0,0]
	v_fma_mix_f32 v12, v97, 1.0, v12 op_sel_hi:[1,0,0]
	v_fma_mix_f32 v13, v97, 1.0, v13 op_sel:[1,0,0] op_sel_hi:[1,0,0]
	s_waitcnt lgkmcnt(0)
	s_add_i32 s18, s18, 10
	s_cmp_ge_i32 s19, s17
	s_cbranch_scc1 .LBB1_309
.LBB1_333:
	s_add_i32 s19, s18, -9
	v_add_lshl_u32 v14, v22, s19, 2
	v_subrev_u32_e32 v15, s19, v57
	v_lshl_add_u32 v32, v2, 7, v31
	s_mov_b32 m0, s5
	global_load_dword v2, v14, s[48:49]
	global_load_lds_dwordx4 v32, s[24:25]
	v_lshl_add_u32 v33, v1, 7, v31
	s_mov_b32 m0, s6
	global_load_dword v1, v14, s[48:49] offset:4
	global_load_lds_dwordx4 v33, s[24:25]
	v_lshl_add_u32 v34, v4, 7, v31
	s_mov_b32 m0, s7
	global_load_dword v4, v14, s[48:49] offset:8
	global_load_lds_dwordx4 v34, s[24:25]
	v_lshl_add_u32 v35, v3, 7, v31
	s_mov_b32 m0, s8
	global_load_dword v3, v14, s[48:49] offset:12
	global_load_lds_dwordx4 v35, s[24:25]
	v_lshl_add_u32 v36, v6, 7, v31
	s_mov_b32 m0, s9
	global_load_dword v6, v14, s[48:49] offset:16
	global_load_lds_dwordx4 v36, s[24:25]
	v_lshl_add_u32 v37, v5, 7, v31
	s_mov_b32 m0, s10
	global_load_dword v5, v14, s[48:49] offset:20
	global_load_lds_dwordx4 v37, s[24:25]
	v_lshl_add_u32 v38, v8, 7, v31
	s_mov_b32 m0, s11
	global_load_dword v8, v14, s[48:49] offset:24
	global_load_lds_dwordx4 v38, s[24:25]
	v_lshl_add_u32 v39, v7, 7, v31
	s_mov_b32 m0, s12
	global_load_dword v7, v14, s[48:49] offset:28
	global_load_lds_dwordx4 v39, s[24:25]
	v_lshl_add_u32 v40, v10, 7, v31
	s_mov_b32 m0, s13
	global_load_dword v10, v14, s[48:49] offset:32
	global_load_lds_dwordx4 v40, s[24:25]
	v_lshl_add_u32 v41, v9, 7, v31
	s_mov_b32 m0, s14
	global_load_dword v9, v14, s[48:49] offset:36
	global_load_lds_dwordx4 v41, s[24:25]
	s_branch .LBB1_332

.LBB1_371:
	s_cmp_eq_u32 s9, 0
	s_cbranch_scc1 .LBB1_392
	s_add_i32 s6, s9, -1
	s_bitcmp1_b32 s6, 0
	s_cselect_b32 s7, 0x2800, 0
	v_add_u32_e32 v59, s7, v1
	ds_read_b128 v[60:63], v59
	ds_read_b128 v[64:67], v59 offset:5120
	s_bitcmp1_b32 s9, 0
	s_cselect_b32 s10, 0x2800, 0
	s_cmp_eq_u32 s6, 23
	s_waitcnt lgkmcnt(1)
	v_mfma_f32_16x16x32_f16 v[70:73], v[2:5], v[60:63], v[18:21]
	v_mfma_f32_16x16x32_f16 v[74:77], v[22:25], v[60:63], v[38:41]
	v_add_u32_e32 v60, s10, v1
	ds_read_b128 v[78:81], v60 offset:20480
	ds_read_b128 v[82:85], v60 offset:25600
	s_cselect_b64 s[10:11], -1, 0
	s_waitcnt lgkmcnt(2)
	v_mfma_f32_16x16x32_f16 v[70:73], v[6:9], v[64:67], v[70:73]
	s_cmp_lg_u32 s6, 23
	v_mfma_f32_16x16x32_f16 v[62:65], v[26:29], v[64:67], v[74:77]
	s_waitcnt lgkmcnt(1)
	v_mfma_f32_16x16x32_f16 v[70:73], v[10:13], v[78:81], v[70:73]
	v_mfma_f32_16x16x32_f16 v[62:65], v[30:33], v[78:81], v[62:65]
	s_waitcnt lgkmcnt(0)
	v_mfma_f32_16x16x32_f16 v[70:73], v[14:17], v[82:85], v[70:73]
	v_mfma_f32_16x16x32_f16 v[62:65], v[34:37], v[82:85], v[62:65]
	ds_read_b128 v[86:89], v59 offset:256
	ds_read_b128 v[90:93], v59 offset:5376
	ds_read_b128 v[94:97], v60 offset:20736
	ds_read_b128 v[98:101], v60 offset:25856
	s_nop 2
	v_exp_f32_e32 v67, v72
	v_exp_f32_e32 v66, v64
	v_exp_f32_e32 v53, v70
	v_exp_f32_e32 v52, v62
	v_exp_f32_e32 v71, v71
	v_exp_f32_e32 v70, v63
	v_pk_add_f32 v[62:63], v[66:67], 1.0 op_sel_hi:[1,0]
	v_pk_fma_f32 v[66:67], v[66:67], s[8:9], v[68:69] op_sel_hi:[1,0,0]
	v_pk_fma_f32 v[52:53], v[52:53], v[62:63], v[62:63]
	v_pk_fma_f32 v[66:67], v[66:67], v[70:71], v[66:67]
	v_fma_f32 v58, v71, v53, v53
	v_fma_f32 v61, v70, v52, v52
	v_rcp_f32_e32 v63, v58
	v_rcp_f32_e32 v62, v61
	v_pk_fma_f32 v[42:43], v[42:43], v[52:53], v[66:67]
	v_exp_f32_e32 v61, v73
	v_exp_f32_e32 v64, v65
	v_pk_mul_f32 v[42:43], v[42:43], v[62:63]
	v_add_u32_e32 v58, s7, v54
	v_exp_f32_e32 v52, v43
	v_exp_f32_e32 v53, v42
	s_nop 0
	v_pk_add_f32 v[52:53], v[52:53], 1.0 op_sel_hi:[1,0]
	s_nop 0
	v_fma_f32 v61, v61, v52, v52
	v_pk_add_f32 v[62:63], v[52:53], 2.0 op_sel_hi:[1,0] neg_lo:[1,0] neg_hi:[1,0]
	v_fmac_f32_e32 v53, v64, v53
	v_rcp_f32_e32 v52, v61
	v_rcp_f32_e32 v53, v53
	s_nop 0
	v_pk_mul_f32 v[52:53], v[62:63], v[52:53]
	s_nop 0
	v_cvt_pk_f16_f32 v61, v52, v53
	ds_write_b32 v58, v61 offset:20480
	s_cbranch_scc0 .Lxt_0
.LBB1_376:
	s_andn2_b64 vcc, exec, s[10:11]
	s_waitcnt lgkmcnt(1)
	v_mfma_f32_16x16x32_f16 v[74:77], v[2:5], v[86:89], v[18:21]
	v_mfma_f32_16x16x32_f16 v[62:65], v[22:25], v[86:89], v[38:41]
	v_mfma_f32_16x16x32_f16 v[74:77], v[6:9], v[90:93], v[74:77]
	v_mfma_f32_16x16x32_f16 v[62:65], v[26:29], v[90:93], v[62:65]
	v_mfma_f32_16x16x32_f16 v[74:77], v[10:13], v[94:97], v[74:77]
	v_mfma_f32_16x16x32_f16 v[62:65], v[30:33], v[94:97], v[62:65]
	v_mfma_f32_16x16x32_f16 v[74:77], v[14:17], v[98:101], v[74:77]
	v_mfma_f32_16x16x32_f16 v[62:65], v[34:37], v[98:101], v[62:65]
	ds_read_b128 v[102:105], v59 offset:512
	ds_read_b128 v[106:109], v59 offset:5632
	ds_read_b128 v[110:113], v60 offset:20992
	ds_read_b128 v[114:117], v60 offset:26112
	s_nop 2
	v_exp_f32_e32 v67, v76
	v_exp_f32_e32 v66, v64
	v_exp_f32_e32 v53, v74
	v_exp_f32_e32 v52, v62
	v_exp_f32_e32 v71, v75
	v_exp_f32_e32 v70, v63
	v_pk_add_f32 v[62:63], v[66:67], 1.0 op_sel_hi:[1,0]
	v_pk_fma_f32 v[66:67], v[66:67], s[8:9], v[68:69] op_sel_hi:[1,0,0]
	v_pk_fma_f32 v[52:53], v[52:53], v[62:63], v[62:63]
	v_pk_fma_f32 v[66:67], v[66:67], v[70:71], v[66:67]
	v_fma_f32 v61, v71, v53, v53
	v_rcp_f32_e32 v63, v61
	v_fma_f32 v61, v70, v52, v52
	v_rcp_f32_e32 v62, v61
	v_pk_fma_f32 v[44:45], v[44:45], v[52:53], v[66:67]
	v_exp_f32_e32 v61, v77
	v_exp_f32_e32 v64, v65
	v_pk_mul_f32 v[44:45], v[44:45], v[62:63]
	s_nop 0
	v_exp_f32_e32 v52, v45
	v_exp_f32_e32 v53, v44
	s_nop 0
	v_pk_add_f32 v[52:53], v[52:53], 1.0 op_sel_hi:[1,0]
	s_nop 0
	v_fma_f32 v61, v61, v52, v52
	v_pk_add_f32 v[62:63], v[52:53], 2.0 op_sel_hi:[1,0] neg_lo:[1,0] neg_hi:[1,0]
	v_fmac_f32_e32 v53, v64, v53
	v_rcp_f32_e32 v52, v61
	v_rcp_f32_e32 v53, v53
	v_cndmask_b32_e64 v61, 0, 1, s[10:11]
	v_cmp_ne_u32_e64 s[6:7], 1, v61
	v_pk_mul_f32 v[52:53], v[62:63], v[52:53]
	s_nop 0
	v_cvt_pk_f16_f32 v61, v52, v53
	ds_write_b32 v58, v61 offset:20736
	s_cbranch_vccz .Lxt_1
.LBB1_380:
	s_and_b64 vcc, exec, s[6:7]
	s_waitcnt lgkmcnt(1)
	v_mfma_f32_16x16x32_f16 v[74:77], v[2:5], v[102:105], v[18:21]
	v_mfma_f32_16x16x32_f16 v[62:65], v[22:25], v[102:105], v[38:41]
	v_mfma_f32_16x16x32_f16 v[74:77], v[6:9], v[106:109], v[74:77]
	v_mfma_f32_16x16x32_f16 v[62:65], v[26:29], v[106:109], v[62:65]
	v_mfma_f32_16x16x32_f16 v[74:77], v[10:13], v[110:113], v[74:77]
	v_mfma_f32_16x16x32_f16 v[62:65], v[30:33], v[110:113], v[62:65]
	v_mfma_f32_16x16x32_f16 v[74:77], v[14:17], v[114:117], v[74:77]
	v_mfma_f32_16x16x32_f16 v[62:65], v[34:37], v[114:117], v[62:65]
	ds_read_b128 v[86:89], v59 offset:768
	ds_read_b128 v[90:93], v59 offset:5888
	ds_read_b128 v[94:97], v60 offset:21248
	ds_read_b128 v[98:101], v60 offset:26368
	s_nop 2
	v_exp_f32_e32 v67, v76
	v_exp_f32_e32 v66, v64
	v_exp_f32_e32 v53, v74
	v_exp_f32_e32 v52, v62
	v_exp_f32_e32 v71, v75
	v_exp_f32_e32 v70, v63
	v_pk_add_f32 v[62:63], v[66:67], 1.0 op_sel_hi:[1,0]
	v_pk_fma_f32 v[66:67], v[66:67], s[8:9], v[68:69] op_sel_hi:[1,0,0]
	v_pk_fma_f32 v[52:53], v[52:53], v[62:63], v[62:63]
	v_pk_fma_f32 v[66:67], v[66:67], v[70:71], v[66:67]
	v_fma_f32 v61, v71, v53, v53
	v_rcp_f32_e32 v63, v61
	v_fma_f32 v61, v70, v52, v52
	v_rcp_f32_e32 v62, v61
	v_pk_fma_f32 v[46:47], v[46:47], v[52:53], v[66:67]
	v_exp_f32_e32 v61, v77
	v_exp_f32_e32 v64, v65
	v_pk_mul_f32 v[46:47], v[46:47], v[62:63]
	s_nop 0
	v_exp_f32_e32 v52, v47
	v_exp_f32_e32 v53, v46
	s_nop 0
	v_pk_add_f32 v[52:53], v[52:53], 1.0 op_sel_hi:[1,0]
	s_nop 0
	v_fma_f32 v61, v61, v52, v52
	v_pk_add_f32 v[62:63], v[52:53], 2.0 op_sel_hi:[1,0] neg_lo:[1,0] neg_hi:[1,0]
	v_fmac_f32_e32 v53, v64, v53
	v_rcp_f32_e32 v52, v61
	v_rcp_f32_e32 v53, v53
	s_nop 0
	v_pk_mul_f32 v[52:53], v[62:63], v[52:53]
	s_nop 0
	v_cvt_pk_f16_f32 v61, v52, v53
	ds_write_b32 v58, v61 offset:20992
	s_cbranch_vccz .Lxt_2
.LBB1_384:
	s_and_b64 vcc, exec, s[6:7]
	s_waitcnt lgkmcnt(1)
	v_mfma_f32_16x16x32_f16 v[74:77], v[2:5], v[86:89], v[18:21]
	v_mfma_f32_16x16x32_f16 v[62:65], v[22:25], v[86:89], v[38:41]
	v_mfma_f32_16x16x32_f16 v[74:77], v[6:9], v[90:93], v[74:77]
	v_mfma_f32_16x16x32_f16 v[62:65], v[26:29], v[90:93], v[62:65]
	v_mfma_f32_16x16x32_f16 v[74:77], v[10:13], v[94:97], v[74:77]
	v_mfma_f32_16x16x32_f16 v[62:65], v[30:33], v[94:97], v[62:65]
	v_mfma_f32_16x16x32_f16 v[74:77], v[14:17], v[98:101], v[74:77]
	v_mfma_f32_16x16x32_f16 v[62:65], v[34:37], v[98:101], v[62:65]
	ds_read_b128 v[102:105], v59 offset:1024
	ds_read_b128 v[106:109], v59 offset:6144
	ds_read_b128 v[110:113], v60 offset:21504
	ds_read_b128 v[114:117], v60 offset:26624
	s_nop 2
	v_exp_f32_e32 v67, v76
	v_exp_f32_e32 v66, v64
	v_exp_f32_e32 v53, v74
	v_exp_f32_e32 v52, v62
	v_exp_f32_e32 v71, v75
	v_exp_f32_e32 v70, v63
	v_pk_add_f32 v[62:63], v[66:67], 1.0 op_sel_hi:[1,0]
	v_pk_fma_f32 v[66:67], v[66:67], s[8:9], v[68:69] op_sel_hi:[1,0,0]
	v_pk_fma_f32 v[52:53], v[52:53], v[62:63], v[62:63]
	v_pk_fma_f32 v[66:67], v[66:67], v[70:71], v[66:67]
	v_fma_f32 v61, v71, v53, v53
	v_rcp_f32_e32 v63, v61
	v_fma_f32 v61, v70, v52, v52
	v_rcp_f32_e32 v62, v61
	v_pk_fma_f32 v[48:49], v[48:49], v[52:53], v[66:67]
	v_exp_f32_e32 v61, v77
	v_exp_f32_e32 v64, v65
	v_pk_mul_f32 v[48:49], v[48:49], v[62:63]
	s_nop 0
	v_exp_f32_e32 v52, v49
	v_exp_f32_e32 v53, v48
	s_nop 0
	v_pk_add_f32 v[52:53], v[52:53], 1.0 op_sel_hi:[1,0]
	s_nop 0
	v_fma_f32 v61, v61, v52, v52
	v_pk_add_f32 v[62:63], v[52:53], 2.0 op_sel_hi:[1,0] neg_lo:[1,0] neg_hi:[1,0]
	v_fmac_f32_e32 v53, v64, v53
	v_rcp_f32_e32 v52, v61
	v_rcp_f32_e32 v53, v53
	s_nop 0
	v_pk_mul_f32 v[52:53], v[62:63], v[52:53]
	s_nop 0
	v_cvt_pk_f16_f32 v61, v52, v53
	ds_write_b32 v58, v61 offset:21248
	s_cbranch_vccz .Lxt_3
.LBB1_388:
	s_and_b64 vcc, exec, s[6:7]
	s_waitcnt lgkmcnt(1)
	v_mfma_f32_16x16x32_f16 v[74:77], v[2:5], v[102:105], v[18:21]
	v_mfma_f32_16x16x32_f16 v[60:63], v[22:25], v[102:105], v[38:41]
	v_mfma_f32_16x16x32_f16 v[74:77], v[6:9], v[106:109], v[74:77]
	v_mfma_f32_16x16x32_f16 v[60:63], v[26:29], v[106:109], v[60:63]
	v_mfma_f32_16x16x32_f16 v[74:77], v[10:13], v[110:113], v[74:77]
	v_mfma_f32_16x16x32_f16 v[60:63], v[30:33], v[110:113], v[60:63]
	v_mfma_f32_16x16x32_f16 v[74:77], v[14:17], v[114:117], v[74:77]
	v_mfma_f32_16x16x32_f16 v[60:63], v[34:37], v[114:117], v[60:63]
	s_nop 6
	v_exp_f32_e32 v65, v76
	v_exp_f32_e32 v64, v62
	v_exp_f32_e32 v53, v74
	v_exp_f32_e32 v52, v60
	v_exp_f32_e32 v67, v75
	v_exp_f32_e32 v66, v61
	v_pk_add_f32 v[60:61], v[64:65], 1.0 op_sel_hi:[1,0]
	v_pk_fma_f32 v[64:65], v[64:65], s[8:9], v[68:69] op_sel_hi:[1,0,0]
	v_pk_fma_f32 v[52:53], v[52:53], v[60:61], v[60:61]
	v_pk_fma_f32 v[64:65], v[64:65], v[66:67], v[64:65]
	v_fma_f32 v59, v67, v53, v53
	v_rcp_f32_e32 v61, v59
	v_fma_f32 v59, v66, v52, v52
	v_rcp_f32_e32 v60, v59
	v_pk_fma_f32 v[50:51], v[50:51], v[52:53], v[64:65]
	v_exp_f32_e32 v59, v77
	v_exp_f32_e32 v62, v63
	v_pk_mul_f32 v[50:51], v[50:51], v[60:61]
	s_nop 0
	v_exp_f32_e32 v52, v51
	v_exp_f32_e32 v53, v50
	s_nop 0
	v_pk_add_f32 v[52:53], v[52:53], 1.0 op_sel_hi:[1,0]
	s_nop 0
	v_fma_f32 v59, v59, v52, v52
	v_pk_add_f32 v[60:61], v[52:53], 2.0 op_sel_hi:[1,0] neg_lo:[1,0] neg_hi:[1,0]
	v_fmac_f32_e32 v53, v62, v53
	v_rcp_f32_e32 v52, v59
	v_rcp_f32_e32 v53, v53
	s_nop 0
	v_pk_mul_f32 v[52:53], v[60:61], v[52:53]
	s_nop 0
	v_cvt_pk_f16_f32 v59, v52, v53
	ds_write_b32 v58, v59 offset:21504
	s_cbranch_vccz .Lxt_4

.Lxt_0:
	v_and_b32_e32 v61, 64, v57
	v_add_f32_e32 v52, v52, v53
	v_xor_b32_e32 v53, 16, v57
	v_add_u32_e32 v61, 64, v61
	v_cmp_lt_i32_e32 vcc, v53, v61
	v_add_f32_e32 v52, 0, v52
	s_nop 0
	v_cndmask_b32_e32 v53, v57, v53, vcc
	v_lshlrev_b32_e32 v53, 2, v53
	ds_bpermute_b32 v53, v53, v52
	s_waitcnt lgkmcnt(0)
	v_add_f32_e32 v52, v52, v53
	v_xor_b32_e32 v53, 32, v57
	v_cmp_lt_i32_e32 vcc, v53, v61
	s_nop 1
	v_cndmask_b32_e32 v53, v57, v53, vcc
	v_lshlrev_b32_e32 v53, 2, v53
	ds_bpermute_b32 v53, v53, v52
	s_and_saveexec_b64 s[6:7], s[4:5]
	s_cbranch_execz .LBB1_375
	s_waitcnt lgkmcnt(0)
	v_add_f32_e32 v52, v52, v53
	v_add_u32_e32 v53, s12, v55
	ds_write_b32 v53, v52
.LBB1_375:
	s_or_b64 exec, exec, s[6:7]
	s_branch .LBB1_376
.Lxt_1:
	v_and_b32_e32 v61, 64, v57
	v_add_f32_e32 v52, v52, v53
	v_xor_b32_e32 v53, 16, v57
	v_add_u32_e32 v61, 64, v61
	v_cmp_lt_i32_e32 vcc, v53, v61
	v_add_f32_e32 v52, 0, v52
	s_nop 0
	v_cndmask_b32_e32 v53, v57, v53, vcc
	v_lshlrev_b32_e32 v53, 2, v53
	ds_bpermute_b32 v53, v53, v52
	s_waitcnt lgkmcnt(0)
	v_add_f32_e32 v52, v52, v53
	v_xor_b32_e32 v53, 32, v57
	v_cmp_lt_i32_e32 vcc, v53, v61
	s_nop 1
	v_cndmask_b32_e32 v53, v57, v53, vcc
	v_lshlrev_b32_e32 v53, 2, v53
	ds_bpermute_b32 v53, v53, v52
	s_and_saveexec_b64 s[10:11], s[4:5]
	s_cbranch_execz .LBB1_379
	s_waitcnt lgkmcnt(0)
	v_add_f32_e32 v52, v52, v53
	v_add_u32_e32 v53, s12, v55
	ds_write_b32 v53, v52 offset:64
.LBB1_379:
	s_or_b64 exec, exec, s[10:11]
	s_branch .LBB1_380
.Lxt_2:
	v_and_b32_e32 v61, 64, v57
	v_add_f32_e32 v52, v52, v53
	v_xor_b32_e32 v53, 16, v57
	v_add_u32_e32 v61, 64, v61
	v_cmp_lt_i32_e32 vcc, v53, v61
	v_add_f32_e32 v52, 0, v52
	s_nop 0
	v_cndmask_b32_e32 v53, v57, v53, vcc
	v_lshlrev_b32_e32 v53, 2, v53
	ds_bpermute_b32 v53, v53, v52
	s_waitcnt lgkmcnt(0)
	v_add_f32_e32 v52, v52, v53
	v_xor_b32_e32 v53, 32, v57
	v_cmp_lt_i32_e32 vcc, v53, v61
	s_nop 1
	v_cndmask_b32_e32 v53, v57, v53, vcc
	v_lshlrev_b32_e32 v53, 2, v53
	ds_bpermute_b32 v53, v53, v52
	s_and_saveexec_b64 s[10:11], s[4:5]
	s_cbranch_execz .LBB1_383
	s_waitcnt lgkmcnt(0)
	v_add_f32_e32 v52, v52, v53
	v_add_u32_e32 v53, s12, v55
	ds_write_b32 v53, v52 offset:128

.Lxt_3:
	v_and_b32_e32 v61, 64, v57
	v_add_f32_e32 v52, v52, v53
	v_xor_b32_e32 v53, 16, v57
	v_add_u32_e32 v61, 64, v61
	v_cmp_lt_i32_e32 vcc, v53, v61
	v_add_f32_e32 v52, 0, v52
	s_nop 0
	v_cndmask_b32_e32 v53, v57, v53, vcc
	v_lshlrev_b32_e32 v53, 2, v53
	ds_bpermute_b32 v53, v53, v52
	s_waitcnt lgkmcnt(0)
	v_add_f32_e32 v52, v52, v53
	v_xor_b32_e32 v53, 32, v57
	v_cmp_lt_i32_e32 vcc, v53, v61
	s_nop 1
	v_cndmask_b32_e32 v53, v57, v53, vcc
	v_lshlrev_b32_e32 v53, 2, v53
	ds_bpermute_b32 v53, v53, v52
	s_and_saveexec_b64 s[10:11], s[4:5]
	s_cbranch_execz .LBB1_387
	s_waitcnt lgkmcnt(0)
	v_add_f32_e32 v52, v52, v53
	v_add_u32_e32 v53, s12, v55
	ds_write_b32 v53, v52 offset:192

.Lxt_4:
	v_and_b32_e32 v58, 64, v57
	v_add_f32_e32 v52, v52, v53
	v_xor_b32_e32 v53, 16, v57
	v_add_u32_e32 v58, 64, v58
	v_cmp_lt_i32_e32 vcc, v53, v58
	v_add_f32_e32 v52, 0, v52
	s_nop 0
	v_cndmask_b32_e32 v53, v57, v53, vcc
	v_lshlrev_b32_e32 v53, 2, v53
	ds_bpermute_b32 v53, v53, v52
	s_waitcnt lgkmcnt(0)
	v_add_f32_e32 v52, v52, v53
	v_xor_b32_e32 v53, 32, v57
	v_cmp_lt_i32_e32 vcc, v53, v58
	s_nop 1
	v_cndmask_b32_e32 v53, v57, v53, vcc
	v_lshlrev_b32_e32 v53, 2, v53
	ds_bpermute_b32 v53, v53, v52
	s_and_saveexec_b64 s[6:7], s[4:5]
	s_cbranch_execz .LBB1_391
	s_waitcnt lgkmcnt(0)
	v_add_f32_e32 v52, v52, v53
	v_add_u32_e32 v53, s12, v55
	ds_write_b32 v53, v52 offset:256
